# barrier: agent-scope invalidate issued by every workgroup right after the leader test (leader publishes first), overlapping the poll; no invalidate after the release
# speedup vs baseline: 1.0054x; 1.0054x over previous
; __device__ __forceinline__ unsigned xb_ld(unsigned* p)              { return __hip_atomic_load(p, __ATOMIC_RELAXED, __HIP_MEMORY_SCOPE_AGENT); }
; __device__ __forceinline__ unsigned xb_add(unsigned* p, unsigned v) { return __hip_atomic_fetch_add(p, v, __ATOMIC_RELAXED, __HIP_MEMORY_SCOPE_AGENT); }
; #define XB_SPIN(cond, bar) do { unsigned _sp = 0; while (cond) { __builtin_amdgcn_s_sleep(1); \
;     if ((++_sp & 255u) == 0u) { if (xb_ld(&(bar)[XB_TMO])) break; if (_sp > XB_SPIN_CAP) { atomicAdd(&(bar)[XB_TMO], 1u); break; } } } } while (0)
; __device__ __forceinline__ void xcd_barrier(const XcdBarrier& b, int wid0) {
;     ...
;         const unsigned old = xb_add(&bar[XB_XSUB(b.x)], 1u);
;         const unsigned gen = old / nloc;
;         if (old + 1u == (gen + 1u) * nloc) {
;             __builtin_amdgcn_fence(__ATOMIC_RELEASE, "agent");
;             asm volatile("s_waitcnt vmcnt(0)" ::: "memory");
;             const unsigned og = xb_add(&bar[XB_TOP], 1u);
;             const unsigned tg = og / nx;
;             if (og + 1u == (tg + 1u) * nx) xb_add(&bar[XB_TOPGEN], 1u);
;             else XB_SPIN(xb_ld(&bar[XB_TOPGEN]) == tg, bar);
;             (void)xb_add(&bar[XB_XGEN(b.x)], 1u);
;             __builtin_amdgcn_fence(__ATOMIC_ACQUIRE, "agent");
;             asm volatile("s_waitcnt vmcnt(0)" ::: "memory");
;         } else {
;             XB_SPIN(xb_ld(&bar[XB_XGEN(b.x)]) == gen, bar);
;             __builtin_amdgcn_fence(__ATOMIC_ACQUIRE, "agent");
;             asm volatile("s_waitcnt vmcnt(0)" ::: "memory");
;         }
.Lxb0_nl:
	buffer_inv sc1
.Lxb0_poll:
	global_load_dword v14, v[10:11], off sc1
	s_add_i32 s8, s8, 1
	s_waitcnt vmcnt(0)
	v_cmp_lt_u32_e32 vcc, v14, v13
	s_nop 1
	s_cbranch_vccz .Lxb0_done
	s_cmp_lt_u32 s8, 0x40000
	s_cbranch_scc0 .Lxb0_done
	s_sleep 1
	s_branch .Lxb0_poll

; __device__ __forceinline__ unsigned xb_ld(unsigned* p)              { return __hip_atomic_load(p, __ATOMIC_RELAXED, __HIP_MEMORY_SCOPE_AGENT); }
; __device__ __forceinline__ unsigned xb_add(unsigned* p, unsigned v) { return __hip_atomic_fetch_add(p, v, __ATOMIC_RELAXED, __HIP_MEMORY_SCOPE_AGENT); }
; #define XB_SPIN(cond, bar) do { unsigned _sp = 0; while (cond) { __builtin_amdgcn_s_sleep(1); \
;     if ((++_sp & 255u) == 0u) { if (xb_ld(&(bar)[XB_TMO])) break; if (_sp > XB_SPIN_CAP) { atomicAdd(&(bar)[XB_TMO], 1u); break; } } } } while (0)
; __device__ __forceinline__ void xcd_barrier(const XcdBarrier& b, int wid0) {
;     ...
;         const unsigned old = xb_add(&bar[XB_XSUB(b.x)], 1u);
;         const unsigned gen = old / nloc;
;         if (old + 1u == (gen + 1u) * nloc) {
;             __builtin_amdgcn_fence(__ATOMIC_RELEASE, "agent");
;             asm volatile("s_waitcnt vmcnt(0)" ::: "memory");
;             const unsigned og = xb_add(&bar[XB_TOP], 1u);
;             const unsigned tg = og / nx;
;             if (og + 1u == (tg + 1u) * nx) xb_add(&bar[XB_TOPGEN], 1u);
;             else XB_SPIN(xb_ld(&bar[XB_TOPGEN]) == tg, bar);
;             (void)xb_add(&bar[XB_XGEN(b.x)], 1u);
;             __builtin_amdgcn_fence(__ATOMIC_ACQUIRE, "agent");
;             asm volatile("s_waitcnt vmcnt(0)" ::: "memory");
;         } else {
;             XB_SPIN(xb_ld(&bar[XB_XGEN(b.x)]) == gen, bar);
;             __builtin_amdgcn_fence(__ATOMIC_ACQUIRE, "agent");
;             asm volatile("s_waitcnt vmcnt(0)" ::: "memory");
;         }
.Lxb1_nl:
	buffer_inv sc1
.Lxb1_poll:
	global_load_dword v14, v[10:11], off sc1
	s_add_i32 s8, s8, 1
	s_waitcnt vmcnt(0)
	v_cmp_lt_u32_e32 vcc, v14, v13
	s_nop 1
	s_cbranch_vccz .Lxb1_done
	s_cmp_lt_u32 s8, 0x40000
	s_cbranch_scc0 .Lxb1_done
	s_sleep 1
	s_branch .Lxb1_poll

; __device__ __forceinline__ unsigned xb_ld(unsigned* p)              { return __hip_atomic_load(p, __ATOMIC_RELAXED, __HIP_MEMORY_SCOPE_AGENT); }
; __device__ __forceinline__ unsigned xb_add(unsigned* p, unsigned v) { return __hip_atomic_fetch_add(p, v, __ATOMIC_RELAXED, __HIP_MEMORY_SCOPE_AGENT); }
; #define XB_SPIN(cond, bar) do { unsigned _sp = 0; while (cond) { __builtin_amdgcn_s_sleep(1); \
;     if ((++_sp & 255u) == 0u) { if (xb_ld(&(bar)[XB_TMO])) break; if (_sp > XB_SPIN_CAP) { atomicAdd(&(bar)[XB_TMO], 1u); break; } } } } while (0)
; __device__ __forceinline__ void xcd_barrier(const XcdBarrier& b, int wid0) {
;     ...
;         const unsigned old = xb_add(&bar[XB_XSUB(b.x)], 1u);
;         const unsigned gen = old / nloc;
;         if (old + 1u == (gen + 1u) * nloc) {
;             __builtin_amdgcn_fence(__ATOMIC_RELEASE, "agent");
;             asm volatile("s_waitcnt vmcnt(0)" ::: "memory");
;             const unsigned og = xb_add(&bar[XB_TOP], 1u);
;             const unsigned tg = og / nx;
;             if (og + 1u == (tg + 1u) * nx) xb_add(&bar[XB_TOPGEN], 1u);
;             else XB_SPIN(xb_ld(&bar[XB_TOPGEN]) == tg, bar);
;             (void)xb_add(&bar[XB_XGEN(b.x)], 1u);
;             __builtin_amdgcn_fence(__ATOMIC_ACQUIRE, "agent");
;             asm volatile("s_waitcnt vmcnt(0)" ::: "memory");
;         } else {
;             XB_SPIN(xb_ld(&bar[XB_XGEN(b.x)]) == gen, bar);
;             __builtin_amdgcn_fence(__ATOMIC_ACQUIRE, "agent");
;             asm volatile("s_waitcnt vmcnt(0)" ::: "memory");
;         }
.Lxb2_nl:
	buffer_inv sc1
.Lxb2_poll:
	global_load_dword v14, v[10:11], off sc1
	s_add_i32 s8, s8, 1
	s_waitcnt vmcnt(0)
	v_cmp_lt_u32_e32 vcc, v14, v13
	s_nop 1
	s_cbranch_vccz .Lxb2_done
	s_cmp_lt_u32 s8, 0x40000
	s_cbranch_scc0 .Lxb2_done
	s_sleep 1
	s_branch .Lxb2_poll

; __device__ __forceinline__ unsigned xb_ld(unsigned* p)              { return __hip_atomic_load(p, __ATOMIC_RELAXED, __HIP_MEMORY_SCOPE_AGENT); }
; __device__ __forceinline__ unsigned xb_add(unsigned* p, unsigned v) { return __hip_atomic_fetch_add(p, v, __ATOMIC_RELAXED, __HIP_MEMORY_SCOPE_AGENT); }
; #define XB_SPIN(cond, bar) do { unsigned _sp = 0; while (cond) { __builtin_amdgcn_s_sleep(1); \
;     if ((++_sp & 255u) == 0u) { if (xb_ld(&(bar)[XB_TMO])) break; if (_sp > XB_SPIN_CAP) { atomicAdd(&(bar)[XB_TMO], 1u); break; } } } } while (0)
; __device__ __forceinline__ void xcd_barrier(const XcdBarrier& b, int wid0) {
;     ...
;         const unsigned old = xb_add(&bar[XB_XSUB(b.x)], 1u);
;         const unsigned gen = old / nloc;
;         if (old + 1u == (gen + 1u) * nloc) {
;             __builtin_amdgcn_fence(__ATOMIC_RELEASE, "agent");
;             asm volatile("s_waitcnt vmcnt(0)" ::: "memory");
;             const unsigned og = xb_add(&bar[XB_TOP], 1u);
;             const unsigned tg = og / nx;
;             if (og + 1u == (tg + 1u) * nx) xb_add(&bar[XB_TOPGEN], 1u);
;             else XB_SPIN(xb_ld(&bar[XB_TOPGEN]) == tg, bar);
;             (void)xb_add(&bar[XB_XGEN(b.x)], 1u);
;             __builtin_amdgcn_fence(__ATOMIC_ACQUIRE, "agent");
;             asm volatile("s_waitcnt vmcnt(0)" ::: "memory");
;         } else {
;             XB_SPIN(xb_ld(&bar[XB_XGEN(b.x)]) == gen, bar);
;             __builtin_amdgcn_fence(__ATOMIC_ACQUIRE, "agent");
;             asm volatile("s_waitcnt vmcnt(0)" ::: "memory");
;         }
.Lxb3_nl:
	buffer_inv sc1
.Lxb3_poll:
	global_load_dword v14, v[10:11], off sc1
	s_add_i32 s8, s8, 1
	s_waitcnt vmcnt(0)
	v_cmp_lt_u32_e32 vcc, v14, v13
	s_nop 1
	s_cbranch_vccz .Lxb3_done
	s_cmp_lt_u32 s8, 0x40000
	s_cbranch_scc0 .Lxb3_done
	s_sleep 1
	s_branch .Lxb3_poll

; __device__ __forceinline__ unsigned xb_ld(unsigned* p)              { return __hip_atomic_load(p, __ATOMIC_RELAXED, __HIP_MEMORY_SCOPE_AGENT); }
; __device__ __forceinline__ unsigned xb_add(unsigned* p, unsigned v) { return __hip_atomic_fetch_add(p, v, __ATOMIC_RELAXED, __HIP_MEMORY_SCOPE_AGENT); }
; #define XB_SPIN(cond, bar) do { unsigned _sp = 0; while (cond) { __builtin_amdgcn_s_sleep(1); \
;     if ((++_sp & 255u) == 0u) { if (xb_ld(&(bar)[XB_TMO])) break; if (_sp > XB_SPIN_CAP) { atomicAdd(&(bar)[XB_TMO], 1u); break; } } } } while (0)
; __device__ __forceinline__ void xcd_barrier(const XcdBarrier& b, int wid0) {
;     ...
;         const unsigned old = xb_add(&bar[XB_XSUB(b.x)], 1u);
;         const unsigned gen = old / nloc;
;         if (old + 1u == (gen + 1u) * nloc) {
;             __builtin_amdgcn_fence(__ATOMIC_RELEASE, "agent");
;             asm volatile("s_waitcnt vmcnt(0)" ::: "memory");
;             const unsigned og = xb_add(&bar[XB_TOP], 1u);
;             const unsigned tg = og / nx;
;             if (og + 1u == (tg + 1u) * nx) xb_add(&bar[XB_TOPGEN], 1u);
;             else XB_SPIN(xb_ld(&bar[XB_TOPGEN]) == tg, bar);
;             (void)xb_add(&bar[XB_XGEN(b.x)], 1u);
;             __builtin_amdgcn_fence(__ATOMIC_ACQUIRE, "agent");
;             asm volatile("s_waitcnt vmcnt(0)" ::: "memory");
;         } else {
;             XB_SPIN(xb_ld(&bar[XB_XGEN(b.x)]) == gen, bar);
;             __builtin_amdgcn_fence(__ATOMIC_ACQUIRE, "agent");
;             asm volatile("s_waitcnt vmcnt(0)" ::: "memory");
;         }
.Lxb4_nl:
	buffer_inv sc1
.Lxb4_poll:
	global_load_dword v14, v[10:11], off sc1
	s_add_i32 s8, s8, 1
	s_waitcnt vmcnt(0)
	v_cmp_lt_u32_e32 vcc, v14, v13
	s_nop 1
	s_cbranch_vccz .Lxb4_done
	s_cmp_lt_u32 s8, 0x40000
	s_cbranch_scc0 .Lxb4_done
	s_sleep 1
	s_branch .Lxb4_poll

; __device__ __forceinline__ unsigned xb_ld(unsigned* p)              { return __hip_atomic_load(p, __ATOMIC_RELAXED, __HIP_MEMORY_SCOPE_AGENT); }
; __device__ __forceinline__ unsigned xb_add(unsigned* p, unsigned v) { return __hip_atomic_fetch_add(p, v, __ATOMIC_RELAXED, __HIP_MEMORY_SCOPE_AGENT); }
; #define XB_SPIN(cond, bar) do { unsigned _sp = 0; while (cond) { __builtin_amdgcn_s_sleep(1); \
;     if ((++_sp & 255u) == 0u) { if (xb_ld(&(bar)[XB_TMO])) break; if (_sp > XB_SPIN_CAP) { atomicAdd(&(bar)[XB_TMO], 1u); break; } } } } while (0)
; __device__ __forceinline__ void xcd_barrier(const XcdBarrier& b, int wid0) {
;     ...
;         const unsigned old = xb_add(&bar[XB_XSUB(b.x)], 1u);
;         const unsigned gen = old / nloc;
;         if (old + 1u == (gen + 1u) * nloc) {
;             __builtin_amdgcn_fence(__ATOMIC_RELEASE, "agent");
;             asm volatile("s_waitcnt vmcnt(0)" ::: "memory");
;             const unsigned og = xb_add(&bar[XB_TOP], 1u);
;             const unsigned tg = og / nx;
;             if (og + 1u == (tg + 1u) * nx) xb_add(&bar[XB_TOPGEN], 1u);
;             else XB_SPIN(xb_ld(&bar[XB_TOPGEN]) == tg, bar);
;             (void)xb_add(&bar[XB_XGEN(b.x)], 1u);
;             __builtin_amdgcn_fence(__ATOMIC_ACQUIRE, "agent");
;             asm volatile("s_waitcnt vmcnt(0)" ::: "memory");
;         } else {
;             XB_SPIN(xb_ld(&bar[XB_XGEN(b.x)]) == gen, bar);
;             __builtin_amdgcn_fence(__ATOMIC_ACQUIRE, "agent");
;             asm volatile("s_waitcnt vmcnt(0)" ::: "memory");
;         }
.Lxb5_nl:
	buffer_inv sc1
.Lxb5_poll:
	global_load_dword v14, v[10:11], off sc1
	s_add_i32 s8, s8, 1
	s_waitcnt vmcnt(0)
	v_cmp_lt_u32_e32 vcc, v14, v13
	s_nop 1
	s_cbranch_vccz .Lxb5_done
	s_cmp_lt_u32 s8, 0x40000
	s_cbranch_scc0 .Lxb5_done
	s_sleep 1
	s_branch .Lxb5_poll

; __device__ __forceinline__ unsigned xb_ld(unsigned* p)              { return __hip_atomic_load(p, __ATOMIC_RELAXED, __HIP_MEMORY_SCOPE_AGENT); }
; __device__ __forceinline__ unsigned xb_add(unsigned* p, unsigned v) { return __hip_atomic_fetch_add(p, v, __ATOMIC_RELAXED, __HIP_MEMORY_SCOPE_AGENT); }
; #define XB_SPIN(cond, bar) do { unsigned _sp = 0; while (cond) { __builtin_amdgcn_s_sleep(1); \
;     if ((++_sp & 255u) == 0u) { if (xb_ld(&(bar)[XB_TMO])) break; if (_sp > XB_SPIN_CAP) { atomicAdd(&(bar)[XB_TMO], 1u); break; } } } } while (0)
; __device__ __forceinline__ void xcd_barrier(const XcdBarrier& b, int wid0) {
;     ...
;         const unsigned old = xb_add(&bar[XB_XSUB(b.x)], 1u);
;         const unsigned gen = old / nloc;
;         if (old + 1u == (gen + 1u) * nloc) {
;             __builtin_amdgcn_fence(__ATOMIC_RELEASE, "agent");
;             asm volatile("s_waitcnt vmcnt(0)" ::: "memory");
;             const unsigned og = xb_add(&bar[XB_TOP], 1u);
;             const unsigned tg = og / nx;
;             if (og + 1u == (tg + 1u) * nx) xb_add(&bar[XB_TOPGEN], 1u);
;             else XB_SPIN(xb_ld(&bar[XB_TOPGEN]) == tg, bar);
;             (void)xb_add(&bar[XB_XGEN(b.x)], 1u);
;             __builtin_amdgcn_fence(__ATOMIC_ACQUIRE, "agent");
;             asm volatile("s_waitcnt vmcnt(0)" ::: "memory");
;         } else {
;             XB_SPIN(xb_ld(&bar[XB_XGEN(b.x)]) == gen, bar);
;             __builtin_amdgcn_fence(__ATOMIC_ACQUIRE, "agent");
;             asm volatile("s_waitcnt vmcnt(0)" ::: "memory");
;         }
.Lxb6_nl:
	buffer_inv sc1
.Lxb6_poll:
	global_load_dword v14, v[10:11], off sc1
	s_add_i32 s8, s8, 1
	s_waitcnt vmcnt(0)
	v_cmp_lt_u32_e32 vcc, v14, v13
	s_nop 1
	s_cbranch_vccz .Lxb6_done
	s_cmp_lt_u32 s8, 0x40000
	s_cbranch_scc0 .Lxb6_done
	s_sleep 1
	s_branch .Lxb6_poll

; __device__ __forceinline__ unsigned xb_ld(unsigned* p)              { return __hip_atomic_load(p, __ATOMIC_RELAXED, __HIP_MEMORY_SCOPE_AGENT); }
; __device__ __forceinline__ unsigned xb_add(unsigned* p, unsigned v) { return __hip_atomic_fetch_add(p, v, __ATOMIC_RELAXED, __HIP_MEMORY_SCOPE_AGENT); }
; #define XB_SPIN(cond, bar) do { unsigned _sp = 0; while (cond) { __builtin_amdgcn_s_sleep(1); \
;     if ((++_sp & 255u) == 0u) { if (xb_ld(&(bar)[XB_TMO])) break; if (_sp > XB_SPIN_CAP) { atomicAdd(&(bar)[XB_TMO], 1u); break; } } } } while (0)
; __device__ __forceinline__ void xcd_barrier(const XcdBarrier& b, int wid0) {
;     ...
;         const unsigned old = xb_add(&bar[XB_XSUB(b.x)], 1u);
;         const unsigned gen = old / nloc;
;         if (old + 1u == (gen + 1u) * nloc) {
;             __builtin_amdgcn_fence(__ATOMIC_RELEASE, "agent");
;             asm volatile("s_waitcnt vmcnt(0)" ::: "memory");
;             const unsigned og = xb_add(&bar[XB_TOP], 1u);
;             const unsigned tg = og / nx;
;             if (og + 1u == (tg + 1u) * nx) xb_add(&bar[XB_TOPGEN], 1u);
;             else XB_SPIN(xb_ld(&bar[XB_TOPGEN]) == tg, bar);
;             (void)xb_add(&bar[XB_XGEN(b.x)], 1u);
;             __builtin_amdgcn_fence(__ATOMIC_ACQUIRE, "agent");
;             asm volatile("s_waitcnt vmcnt(0)" ::: "memory");
;         } else {
;             XB_SPIN(xb_ld(&bar[XB_XGEN(b.x)]) == gen, bar);
;             __builtin_amdgcn_fence(__ATOMIC_ACQUIRE, "agent");
;             asm volatile("s_waitcnt vmcnt(0)" ::: "memory");
;         }
.Lxb7_nl:
	buffer_inv sc1
.Lxb7_poll:
	global_load_dword v14, v[10:11], off sc1
	s_add_i32 s8, s8, 1
	s_waitcnt vmcnt(0)
	v_cmp_lt_u32_e32 vcc, v14, v13
	s_nop 1
	s_cbranch_vccz .Lxb7_done
	s_cmp_lt_u32 s8, 0x40000
	s_cbranch_scc0 .Lxb7_done
	s_sleep 1
	s_branch .Lxb7_poll

; __device__ __forceinline__ unsigned xb_ld(unsigned* p)              { return __hip_atomic_load(p, __ATOMIC_RELAXED, __HIP_MEMORY_SCOPE_AGENT); }
; __device__ __forceinline__ unsigned xb_add(unsigned* p, unsigned v) { return __hip_atomic_fetch_add(p, v, __ATOMIC_RELAXED, __HIP_MEMORY_SCOPE_AGENT); }
; #define XB_SPIN(cond, bar) do { unsigned _sp = 0; while (cond) { __builtin_amdgcn_s_sleep(1); \
;     if ((++_sp & 255u) == 0u) { if (xb_ld(&(bar)[XB_TMO])) break; if (_sp > XB_SPIN_CAP) { atomicAdd(&(bar)[XB_TMO], 1u); break; } } } } while (0)
; __device__ __forceinline__ void xcd_barrier(const XcdBarrier& b, int wid0) {
;     ...
;         const unsigned old = xb_add(&bar[XB_XSUB(b.x)], 1u);
;         const unsigned gen = old / nloc;
;         if (old + 1u == (gen + 1u) * nloc) {
;             __builtin_amdgcn_fence(__ATOMIC_RELEASE, "agent");
;             asm volatile("s_waitcnt vmcnt(0)" ::: "memory");
;             const unsigned og = xb_add(&bar[XB_TOP], 1u);
;             const unsigned tg = og / nx;
;             if (og + 1u == (tg + 1u) * nx) xb_add(&bar[XB_TOPGEN], 1u);
;             else XB_SPIN(xb_ld(&bar[XB_TOPGEN]) == tg, bar);
;             (void)xb_add(&bar[XB_XGEN(b.x)], 1u);
;             __builtin_amdgcn_fence(__ATOMIC_ACQUIRE, "agent");
;             asm volatile("s_waitcnt vmcnt(0)" ::: "memory");
;         } else {
;             XB_SPIN(xb_ld(&bar[XB_XGEN(b.x)]) == gen, bar);
;             __builtin_amdgcn_fence(__ATOMIC_ACQUIRE, "agent");
;             asm volatile("s_waitcnt vmcnt(0)" ::: "memory");
;         }
.Lxb8_nl:
	buffer_inv sc1
.Lxb8_poll:
	global_load_dword v14, v[10:11], off sc1
	s_add_i32 s8, s8, 1
	s_waitcnt vmcnt(0)
	v_cmp_lt_u32_e32 vcc, v14, v13
	s_nop 1
	s_cbranch_vccz .Lxb8_done
	s_cmp_lt_u32 s8, 0x40000
	s_cbranch_scc0 .Lxb8_done
	s_sleep 1
	s_branch .Lxb8_poll

; __device__ __forceinline__ unsigned xb_ld(unsigned* p)              { return __hip_atomic_load(p, __ATOMIC_RELAXED, __HIP_MEMORY_SCOPE_AGENT); }
; __device__ __forceinline__ unsigned xb_add(unsigned* p, unsigned v) { return __hip_atomic_fetch_add(p, v, __ATOMIC_RELAXED, __HIP_MEMORY_SCOPE_AGENT); }
; #define XB_SPIN(cond, bar) do { unsigned _sp = 0; while (cond) { __builtin_amdgcn_s_sleep(1); \
;     if ((++_sp & 255u) == 0u) { if (xb_ld(&(bar)[XB_TMO])) break; if (_sp > XB_SPIN_CAP) { atomicAdd(&(bar)[XB_TMO], 1u); break; } } } } while (0)
; __device__ __forceinline__ void xcd_barrier(const XcdBarrier& b, int wid0) {
;     ...
;         const unsigned old = xb_add(&bar[XB_XSUB(b.x)], 1u);
;         const unsigned gen = old / nloc;
;         if (old + 1u == (gen + 1u) * nloc) {
;             __builtin_amdgcn_fence(__ATOMIC_RELEASE, "agent");
;             asm volatile("s_waitcnt vmcnt(0)" ::: "memory");
;             const unsigned og = xb_add(&bar[XB_TOP], 1u);
;             const unsigned tg = og / nx;
;             if (og + 1u == (tg + 1u) * nx) xb_add(&bar[XB_TOPGEN], 1u);
;             else XB_SPIN(xb_ld(&bar[XB_TOPGEN]) == tg, bar);
;             (void)xb_add(&bar[XB_XGEN(b.x)], 1u);
;             __builtin_amdgcn_fence(__ATOMIC_ACQUIRE, "agent");
;             asm volatile("s_waitcnt vmcnt(0)" ::: "memory");
;         } else {
;             XB_SPIN(xb_ld(&bar[XB_XGEN(b.x)]) == gen, bar);
;             __builtin_amdgcn_fence(__ATOMIC_ACQUIRE, "agent");
;             asm volatile("s_waitcnt vmcnt(0)" ::: "memory");
;         }
.Lxb9_nl:
	buffer_inv sc1
.Lxb9_poll:
	global_load_dword v14, v[10:11], off sc1
	s_add_i32 s8, s8, 1
	s_waitcnt vmcnt(0)
	v_cmp_lt_u32_e32 vcc, v14, v13
	s_nop 1
	s_cbranch_vccz .Lxb9_done
	s_cmp_lt_u32 s8, 0x40000
	s_cbranch_scc0 .Lxb9_done
	s_sleep 1
	s_branch .Lxb9_poll
